# tconv8 epilogue operand loads (u, gate) also fetched as full 128-byte lines (8 rows per instruction, saddr form) and redistributed through wave-private LDS to the MFMA output layout
# speedup vs baseline: 1.0243x; 1.0043x over previous
.LBB0_539:
	s_add_i32 s5, s4, 0x80
	s_and_b32 s72, s5, 0xf80
	v_lshl_add_u64 v[168:169], v[188:189], 0, s[72:73]
	global_load_dwordx4 v[172:175], v[168:169], off
	s_nop 0
	global_load_dwordx4 v[168:171], v[168:169], off offset:16
	v_add_u32_e32 v185, s4, v192
	v_add_u32_e32 v203, s72, v192
	ds_read_b128 v[204:207], v185 offset:320
	ds_read_b128 v[208:211], v185 offset:336
	ds_read_b128 v[212:215], v185 offset:352
	ds_read_b128 v[216:219], v185 offset:368
	ds_read_b128 v[220:223], v185 offset:384
	ds_read_b128 v[224:227], v185 offset:400
	ds_read_b128 v[228:231], v185 offset:416
	s_waitcnt vmcnt(2) lgkmcnt(7)
	v_mfma_f32_16x16x128_f8f6f4 v[164:167], v[28:35], v[0:7], v[164:167]
	v_mfma_f32_16x16x128_f8f6f4 v[160:163], v[24:31], v[0:7], v[160:163]
	v_mfma_f32_16x16x128_f8f6f4 v[156:159], v[20:27], v[0:7], v[156:159]
	v_mfma_f32_16x16x128_f8f6f4 v[152:155], v[16:23], v[0:7], v[152:155]
	v_mfma_f32_16x16x128_f8f6f4 v[148:151], v[12:19], v[0:7], v[148:151]
	v_mfma_f32_16x16x128_f8f6f4 v[144:147], v[8:15], v[0:7], v[144:147]
	ds_read_b128 v[8:11], v185 offset:240
	ds_read_b128 v[12:15], v185 offset:256
	ds_read_b128 v[16:19], v185 offset:272
	ds_read_b128 v[20:23], v185 offset:288
	ds_read_b128 v[24:27], v185 offset:304
	ds_read_b128 v[28:31], v185 offset:320
	s_waitcnt lgkmcnt(6)
	v_mfma_f32_16x16x128_f8f6f4 v[140:143], v[224:231], v[0:7], v[140:143]
	v_mfma_f32_16x16x128_f8f6f4 v[136:139], v[220:227], v[0:7], v[136:139]
	v_mfma_f32_16x16x128_f8f6f4 v[132:135], v[216:223], v[0:7], v[132:135]
	v_mfma_f32_16x16x128_f8f6f4 v[128:131], v[212:219], v[0:7], v[128:131]
	v_mfma_f32_16x16x128_f8f6f4 v[124:127], v[208:215], v[0:7], v[124:127]
	v_mfma_f32_16x16x128_f8f6f4 v[120:123], v[204:211], v[0:7], v[120:123]
	ds_read_b128 v[204:207], v185 offset:160
	ds_read_b128 v[208:211], v185 offset:176
	ds_read_b128 v[212:215], v185 offset:192
	ds_read_b128 v[216:219], v185 offset:208
	ds_read_b128 v[220:223], v185 offset:224
	ds_read_b128 v[224:227], v185 offset:240
	s_waitcnt lgkmcnt(6)
	v_mfma_f32_16x16x128_f8f6f4 v[116:119], v[24:31], v[0:7], v[116:119]
	v_mfma_f32_16x16x128_f8f6f4 v[112:115], v[20:27], v[0:7], v[112:115]
	v_mfma_f32_16x16x128_f8f6f4 v[108:111], v[16:23], v[0:7], v[108:111]
	v_mfma_f32_16x16x128_f8f6f4 v[104:107], v[12:19], v[0:7], v[104:107]
	v_mfma_f32_16x16x128_f8f6f4 v[100:103], v[8:15], v[0:7], v[100:103]
	ds_read_b128 v[8:11], v185 offset:80
	ds_read_b128 v[12:15], v185 offset:96
	ds_read_b128 v[16:19], v185 offset:112
	ds_read_b128 v[20:23], v185 offset:128
	ds_read_b128 v[24:27], v185 offset:144
	ds_read_b128 v[28:31], v185 offset:160
	s_waitcnt lgkmcnt(6)
	v_mfma_f32_16x16x128_f8f6f4 v[96:99], v[220:227], v[0:7], v[96:99]
	v_mfma_f32_16x16x128_f8f6f4 v[92:95], v[216:223], v[0:7], v[92:95]
	v_mfma_f32_16x16x128_f8f6f4 v[88:91], v[212:219], v[0:7], v[88:91]
	v_mfma_f32_16x16x128_f8f6f4 v[84:87], v[208:215], v[0:7], v[84:87]
	v_mfma_f32_16x16x128_f8f6f4 v[80:83], v[204:211], v[0:7], v[80:83]
	ds_read_b128 v[204:207], v185 offset:0
	ds_read_b128 v[208:211], v185 offset:16
	ds_read_b128 v[212:215], v185 offset:32
	ds_read_b128 v[216:219], v185 offset:48
	ds_read_b128 v[220:223], v185 offset:64
	ds_read_b128 v[224:227], v185 offset:80
	s_waitcnt lgkmcnt(6)
	v_mfma_f32_16x16x128_f8f6f4 v[76:79], v[24:31], v[0:7], v[76:79]
	v_mfma_f32_16x16x128_f8f6f4 v[72:75], v[20:27], v[0:7], v[72:75]
	v_mfma_f32_16x16x128_f8f6f4 v[68:71], v[16:23], v[0:7], v[68:71]
	v_mfma_f32_16x16x128_f8f6f4 v[64:67], v[12:19], v[0:7], v[64:67]
	v_mfma_f32_16x16x128_f8f6f4 v[60:63], v[8:15], v[0:7], v[60:63]
	ds_read_b128 v[8:11], v203 offset:416
	ds_read_b128 v[12:15], v203 offset:432
	ds_read_b128 v[16:19], v203 offset:448
	ds_read_b128 v[20:23], v203 offset:464
	ds_read_b128 v[24:27], v203 offset:480
	ds_read_b128 v[28:31], v203 offset:496
	ds_read_b128 v[32:35], v203 offset:512
	s_waitcnt lgkmcnt(7)
	v_mfma_f32_16x16x128_f8f6f4 v[56:59], v[220:227], v[0:7], v[56:59]
	v_mfma_f32_16x16x128_f8f6f4 v[52:55], v[216:223], v[0:7], v[52:55]
	v_mfma_f32_16x16x128_f8f6f4 v[48:51], v[212:219], v[0:7], v[48:51]
	v_mfma_f32_16x16x128_f8f6f4 v[44:47], v[208:215], v[0:7], v[44:47]
	v_mfma_f32_16x16x128_f8f6f4 v[40:43], v[204:211], v[0:7], v[40:43]
	s_cmpk_eq_i32 s5, 0x1000
	s_mov_b32 s4, s5
	s_waitcnt vmcnt(0)
	v_mov_b32_e32 v0, v172
	v_mov_b32_e32 v1, v173
	v_mov_b32_e32 v2, v174
	v_mov_b32_e32 v3, v175
	v_mov_b32_e32 v4, v168
	v_mov_b32_e32 v5, v169
	v_mov_b32_e32 v6, v170
	v_mov_b32_e32 v7, v171
	s_cbranch_scc0 .LBB0_539
	s_waitcnt lgkmcnt(0)
	s_barrier
	s_lshl_b64 s[4:5], s[36:37], 2
	s_add_u32 s4, s31, s4
	s_addc_u32 s5, s46, s5
	global_load_dword v4, v245, s[4:5]
	v_lshl_add_u64 v[0:1], v[186:187], 0, v[182:183]
	v_lshlrev_b64 v[2:3], 1, v[0:1]
	v_mbcnt_lo_u32_b32 v5, -1, 0
	v_mbcnt_hi_u32_b32 v5, -1, v5
	v_and_b32_e32 v38, 15, v5
	v_lshrrev_b32_e32 v39, 4, v5
	v_lshrrev_b32_e32 v246, 3, v5
	v_and_b32_e32 v247, 7, v5
	v_sub_u32_e32 v248, v246, v38
	v_mul_i32_i24_e32 v249, 0x600000, v248
	v_lshlrev_b32_e32 v250, 3, v39
	v_sub_u32_e32 v249, v249, v250
	v_lshlrev_b32_e32 v251, 4, v247
	v_add_u32_e32 v198, v249, v251
	v_add_u32_e32 v201, v2, v198
	v_add_u32_e32 v202, 0x3000000, v201
	global_load_dwordx4 v[204:207], v201, s[22:23]
	global_load_dwordx4 v[208:211], v201, s[22:23] offset:128
	global_load_dwordx4 v[212:215], v202, s[22:23]
	global_load_dwordx4 v[216:219], v202, s[22:23] offset:128
	global_load_dwordx4 v[220:223], v201, s[24:25]
	global_load_dwordx4 v[224:227], v201, s[24:25] offset:128
	global_load_dwordx4 v[228:231], v202, s[24:25]
	global_load_dwordx4 v[232:235], v202, s[24:25] offset:128
	v_ashrrev_i32_e32 v199, 31, v198
	v_lshl_add_u64 v[2:3], s[26:27], 0, v[2:3]
	v_lshl_add_u64 v[0:1], s[28:29], 0, v[0:1]
	v_lshl_add_u64 v[194:195], v[198:199], 0, v[2:3]
	v_mov_b32_e32 v198, 0x3000000
	v_mov_b32_e32 v199, 0
	v_lshl_add_u64 v[196:197], v[198:199], 0, v[194:195]
	v_mul_i32_i24_e32 v249, 0x300000, v248
	v_lshlrev_b32_e32 v250, 2, v39
	v_sub_u32_e32 v249, v249, v250
	v_add_u32_e32 v198, v249, v251
	v_ashrrev_i32_e32 v199, 31, v198
	v_lshl_add_u64 v[2:3], v[198:199], 0, v[0:1]
	v_mov_b32_e32 v198, 0x1800000
	v_mov_b32_e32 v199, 0
	v_lshl_add_u64 v[198:199], v[198:199], 0, v[2:3]
	v_lshrrev_b32_e32 v250, 6, v200
	v_mul_u32_u24_e32 v249, 0x1200, v250
	v_mul_u32_u24_e32 v248, 0x90, v38
	v_add_u32_e32 v248, v248, v249
	v_lshl_add_u32 v0, v39, 3, v248
	v_mul_u32_u24_e32 v243, 0x110, v38
	v_mul_u32_u24_e32 v5, 0x2200, v250
	v_add_u32_e32 v5, 0xa000, v5
	v_add_u32_e32 v243, v243, v5
	v_lshl_add_u32 v243, v39, 3, v243
	v_mul_u32_u24_e32 v242, 0x110, v246
	v_add_u32_e32 v242, v242, v5
	v_add_u32_e32 v242, v242, v251
	v_lshl_add_u32 v38, v39, 2, v248
	v_add_u32_e32 v38, 0x900, v38
	v_mul_u32_u24_e32 v246, 0x90, v246
	v_add_u32_e32 v246, v246, v249
	v_add_u32_e32 v1, v246, v251
	v_add_u32_e32 v39, 0x900, v1
	v_mov_b32_e32 v252, 0x43dc0000
	s_and_b64 vcc, exec, s[34:35]
	s_waitcnt vmcnt(0)
	ds_write_b128 v242, v[204:207]
	ds_write_b128 v242, v[208:211] offset:128
	ds_write_b128 v242, v[212:215] offset:2176
	ds_write_b128 v242, v[216:219] offset:2304
	ds_write_b128 v242, v[220:223] offset:4352
	ds_write_b128 v242, v[224:227] offset:4480
	ds_write_b128 v242, v[228:231] offset:6528
	ds_write_b128 v242, v[232:235] offset:6656
	global_load_dwordx4 v[204:207], v201, s[22:23] offset:256
	global_load_dwordx4 v[208:211], v201, s[22:23] offset:384
	global_load_dwordx4 v[212:215], v202, s[22:23] offset:256
	global_load_dwordx4 v[216:219], v202, s[22:23] offset:384
	global_load_dwordx4 v[220:223], v201, s[24:25] offset:256
	global_load_dwordx4 v[224:227], v201, s[24:25] offset:384
	global_load_dwordx4 v[228:231], v202, s[24:25] offset:256
	global_load_dwordx4 v[232:235], v202, s[24:25] offset:384
	s_waitcnt lgkmcnt(0)
	ds_read_b64 v[10:11], v243
	ds_read_b64 v[12:13], v243 offset:4352
	ds_read_b64 v[14:15], v243 offset:32
	ds_read_b64 v[16:17], v243 offset:4384
	ds_read_b64 v[18:19], v243 offset:64
	ds_read_b64 v[20:21], v243 offset:4416
	ds_read_b64 v[22:23], v243 offset:96
	ds_read_b64 v[24:25], v243 offset:4448
	ds_read_b64 v[26:27], v243 offset:128
	ds_read_b64 v[28:29], v243 offset:4480
	ds_read_b64 v[30:31], v243 offset:160
	ds_read_b64 v[32:33], v243 offset:4512
	ds_read_b64 v[34:35], v243 offset:192
	ds_read_b64 v[36:37], v243 offset:4544
	ds_read_b64 v[236:237], v243 offset:224
	ds_read_b64 v[238:239], v243 offset:4576
	s_waitcnt lgkmcnt(0)
	v_lshlrev_b32_e32 v168, 16, v10
	v_and_b32_e32 v169, 0xffff0000, v10
	v_lshlrev_b32_e32 v170, 16, v11
	v_and_b32_e32 v171, 0xffff0000, v11
	v_lshlrev_b32_e32 v172, 16, v12
	v_and_b32_e32 v173, 0xffff0000, v12
	v_lshlrev_b32_e32 v174, 16, v13
	v_and_b32_e32 v175, 0xffff0000, v13
	v_pk_mul_f32 v[168:169], v[4:5], v[168:169] op_sel_hi:[0,1]
	v_pk_mul_f32 v[170:171], v[4:5], v[170:171] op_sel_hi:[0,1]
	v_pk_fma_f32 v[164:165], v[184:185], v[164:165], v[168:169] op_sel_hi:[0,1,1]
	v_pk_fma_f32 v[166:167], v[184:185], v[166:167], v[170:171] op_sel_hi:[0,1,1]
	v_pk_mul_f32 v[164:165], v[164:165], v[172:173]
	v_pk_mul_f32 v[166:167], v[166:167], v[174:175]
	v_cvt_pk_bf16_f32 v240, v164, v165
	v_cvt_pk_bf16_f32 v241, v166, v167
	ds_write_b64 v0, v[240:241]
	v_lshlrev_b32_e32 v168, 16, v14
	v_and_b32_e32 v169, 0xffff0000, v14
	v_lshlrev_b32_e32 v170, 16, v15
	v_and_b32_e32 v171, 0xffff0000, v15
	v_lshlrev_b32_e32 v172, 16, v16
	v_and_b32_e32 v173, 0xffff0000, v16
	v_lshlrev_b32_e32 v174, 16, v17
	v_and_b32_e32 v175, 0xffff0000, v17
	v_pk_mul_f32 v[168:169], v[4:5], v[168:169] op_sel_hi:[0,1]
	v_pk_mul_f32 v[170:171], v[4:5], v[170:171] op_sel_hi:[0,1]
	v_pk_fma_f32 v[160:161], v[184:185], v[160:161], v[168:169] op_sel_hi:[0,1,1]
	v_pk_fma_f32 v[162:163], v[184:185], v[162:163], v[170:171] op_sel_hi:[0,1,1]
	v_pk_mul_f32 v[160:161], v[160:161], v[172:173]
	v_pk_mul_f32 v[162:163], v[162:163], v[174:175]
	v_cvt_pk_bf16_f32 v240, v160, v161
	v_cvt_pk_bf16_f32 v241, v162, v163
	ds_write_b64 v0, v[240:241] offset:32
	v_lshlrev_b32_e32 v168, 16, v18
	v_and_b32_e32 v169, 0xffff0000, v18
	v_lshlrev_b32_e32 v170, 16, v19
	v_and_b32_e32 v171, 0xffff0000, v19
	v_lshlrev_b32_e32 v172, 16, v20
	v_and_b32_e32 v173, 0xffff0000, v20
	v_lshlrev_b32_e32 v174, 16, v21
	v_and_b32_e32 v175, 0xffff0000, v21
	v_pk_mul_f32 v[168:169], v[4:5], v[168:169] op_sel_hi:[0,1]
	v_pk_mul_f32 v[170:171], v[4:5], v[170:171] op_sel_hi:[0,1]
	v_pk_fma_f32 v[156:157], v[184:185], v[156:157], v[168:169] op_sel_hi:[0,1,1]
	v_pk_fma_f32 v[158:159], v[184:185], v[158:159], v[170:171] op_sel_hi:[0,1,1]
	v_pk_mul_f32 v[156:157], v[156:157], v[172:173]
	v_pk_mul_f32 v[158:159], v[158:159], v[174:175]
	v_cvt_pk_bf16_f32 v240, v156, v157
	v_cvt_pk_bf16_f32 v241, v158, v159
	ds_write_b64 v0, v[240:241] offset:64
	v_lshlrev_b32_e32 v168, 16, v22
	v_and_b32_e32 v169, 0xffff0000, v22
	v_lshlrev_b32_e32 v170, 16, v23
	v_and_b32_e32 v171, 0xffff0000, v23
	v_lshlrev_b32_e32 v172, 16, v24
	v_and_b32_e32 v173, 0xffff0000, v24
	v_lshlrev_b32_e32 v174, 16, v25
	v_and_b32_e32 v175, 0xffff0000, v25
	v_pk_mul_f32 v[168:169], v[4:5], v[168:169] op_sel_hi:[0,1]
	v_pk_mul_f32 v[170:171], v[4:5], v[170:171] op_sel_hi:[0,1]
	v_pk_fma_f32 v[152:153], v[184:185], v[152:153], v[168:169] op_sel_hi:[0,1,1]
	v_pk_fma_f32 v[154:155], v[184:185], v[154:155], v[170:171] op_sel_hi:[0,1,1]
	v_pk_mul_f32 v[152:153], v[152:153], v[172:173]
	v_pk_mul_f32 v[154:155], v[154:155], v[174:175]
	v_cvt_pk_bf16_f32 v240, v152, v153
	v_cvt_pk_bf16_f32 v241, v154, v155
	ds_write_b64 v0, v[240:241] offset:96
	ds_read_b128 v[168:171], v1
	ds_read_b128 v[172:175], v1 offset:1152
	s_cbranch_vccz .Lt8z_0_0
	v_med3_f32 v248, v164, s77, v252
	v_med3_f32 v249, v165, s77, v252
	v_med3_f32 v250, v166, s77, v252
	v_med3_f32 v251, v167, s77, v252
	v_mov_b32_e32 v246, v245
	v_cvt_pk_fp8_f32 v246, v248, v249
	v_cvt_pk_fp8_f32 v246, v250, v251 op_sel:[0,0,1]
	ds_write_b32 v38, v246
	v_med3_f32 v248, v160, s77, v252
	v_med3_f32 v249, v161, s77, v252
	v_med3_f32 v250, v162, s77, v252
	v_med3_f32 v251, v163, s77, v252
	v_mov_b32_e32 v246, v245
	v_cvt_pk_fp8_f32 v246, v248, v249
	v_cvt_pk_fp8_f32 v246, v250, v251 op_sel:[0,0,1]
	ds_write_b32 v38, v246 offset:16
	v_med3_f32 v248, v156, s77, v252
	v_med3_f32 v249, v157, s77, v252
	v_med3_f32 v250, v158, s77, v252
	v_med3_f32 v251, v159, s77, v252
	v_mov_b32_e32 v246, v245
	v_cvt_pk_fp8_f32 v246, v248, v249
	v_cvt_pk_fp8_f32 v246, v250, v251 op_sel:[0,0,1]
	ds_write_b32 v38, v246 offset:32
	v_med3_f32 v248, v152, s77, v252
	v_med3_f32 v249, v153, s77, v252
	v_med3_f32 v250, v154, s77, v252
	v_med3_f32 v251, v155, s77, v252
	v_mov_b32_e32 v246, v245
	v_cvt_pk_fp8_f32 v246, v248, v249
	v_cvt_pk_fp8_f32 v246, v250, v251 op_sel:[0,0,1]
	ds_write_b32 v38, v246 offset:48
.Lt8z_0_0:
	s_waitcnt lgkmcnt(0)
	global_store_dwordx4 v[194:195], v[168:171], off
	global_store_dwordx4 v[196:197], v[172:175], off
	s_nop 1
	v_lshlrev_b32_e32 v168, 16, v26
	v_and_b32_e32 v169, 0xffff0000, v26
	v_lshlrev_b32_e32 v170, 16, v27
	v_and_b32_e32 v171, 0xffff0000, v27
	v_lshlrev_b32_e32 v172, 16, v28
	v_and_b32_e32 v173, 0xffff0000, v28
	v_lshlrev_b32_e32 v174, 16, v29
	v_and_b32_e32 v175, 0xffff0000, v29
	v_pk_mul_f32 v[168:169], v[4:5], v[168:169] op_sel_hi:[0,1]
	v_pk_mul_f32 v[170:171], v[4:5], v[170:171] op_sel_hi:[0,1]
	v_pk_fma_f32 v[148:149], v[184:185], v[148:149], v[168:169] op_sel_hi:[0,1,1]
	v_pk_fma_f32 v[150:151], v[184:185], v[150:151], v[170:171] op_sel_hi:[0,1,1]
	v_pk_mul_f32 v[148:149], v[148:149], v[172:173]
	v_pk_mul_f32 v[150:151], v[150:151], v[174:175]
	v_cvt_pk_bf16_f32 v240, v148, v149
	v_cvt_pk_bf16_f32 v241, v150, v151
	ds_write_b64 v0, v[240:241]
	v_lshlrev_b32_e32 v168, 16, v30
	v_and_b32_e32 v169, 0xffff0000, v30
	v_lshlrev_b32_e32 v170, 16, v31
	v_and_b32_e32 v171, 0xffff0000, v31
	v_lshlrev_b32_e32 v172, 16, v32
	v_and_b32_e32 v173, 0xffff0000, v32
	v_lshlrev_b32_e32 v174, 16, v33
	v_and_b32_e32 v175, 0xffff0000, v33
	v_pk_mul_f32 v[168:169], v[4:5], v[168:169] op_sel_hi:[0,1]
	v_pk_mul_f32 v[170:171], v[4:5], v[170:171] op_sel_hi:[0,1]
	v_pk_fma_f32 v[144:145], v[184:185], v[144:145], v[168:169] op_sel_hi:[0,1,1]
	v_pk_fma_f32 v[146:147], v[184:185], v[146:147], v[170:171] op_sel_hi:[0,1,1]
	v_pk_mul_f32 v[144:145], v[144:145], v[172:173]
	v_pk_mul_f32 v[146:147], v[146:147], v[174:175]
	v_cvt_pk_bf16_f32 v240, v144, v145
	v_cvt_pk_bf16_f32 v241, v146, v147
	ds_write_b64 v0, v[240:241] offset:32
	v_lshlrev_b32_e32 v168, 16, v34
	v_and_b32_e32 v169, 0xffff0000, v34
	v_lshlrev_b32_e32 v170, 16, v35
	v_and_b32_e32 v171, 0xffff0000, v35
	v_lshlrev_b32_e32 v172, 16, v36
	v_and_b32_e32 v173, 0xffff0000, v36
	v_lshlrev_b32_e32 v174, 16, v37
	v_and_b32_e32 v175, 0xffff0000, v37
	v_pk_mul_f32 v[168:169], v[4:5], v[168:169] op_sel_hi:[0,1]
	v_pk_mul_f32 v[170:171], v[4:5], v[170:171] op_sel_hi:[0,1]
	v_pk_fma_f32 v[140:141], v[184:185], v[140:141], v[168:169] op_sel_hi:[0,1,1]
	v_pk_fma_f32 v[142:143], v[184:185], v[142:143], v[170:171] op_sel_hi:[0,1,1]
	v_pk_mul_f32 v[140:141], v[140:141], v[172:173]
	v_pk_mul_f32 v[142:143], v[142:143], v[174:175]
	v_cvt_pk_bf16_f32 v240, v140, v141
	v_cvt_pk_bf16_f32 v241, v142, v143
	ds_write_b64 v0, v[240:241] offset:64
	v_lshlrev_b32_e32 v168, 16, v236
	v_and_b32_e32 v169, 0xffff0000, v236
	v_lshlrev_b32_e32 v170, 16, v237
	v_and_b32_e32 v171, 0xffff0000, v237
	v_lshlrev_b32_e32 v172, 16, v238
	v_and_b32_e32 v173, 0xffff0000, v238
	v_lshlrev_b32_e32 v174, 16, v239
	v_and_b32_e32 v175, 0xffff0000, v239
	v_pk_mul_f32 v[168:169], v[4:5], v[168:169] op_sel_hi:[0,1]
	v_pk_mul_f32 v[170:171], v[4:5], v[170:171] op_sel_hi:[0,1]
	v_pk_fma_f32 v[136:137], v[184:185], v[136:137], v[168:169] op_sel_hi:[0,1,1]
	v_pk_fma_f32 v[138:139], v[184:185], v[138:139], v[170:171] op_sel_hi:[0,1,1]
	v_pk_mul_f32 v[136:137], v[136:137], v[172:173]
	v_pk_mul_f32 v[138:139], v[138:139], v[174:175]
	v_cvt_pk_bf16_f32 v240, v136, v137
	v_cvt_pk_bf16_f32 v241, v138, v139
	ds_write_b64 v0, v[240:241] offset:96
	ds_read_b128 v[168:171], v1
	ds_read_b128 v[172:175], v1 offset:1152
	s_cbranch_vccz .Lt8z_0_1
	v_med3_f32 v248, v148, s77, v252
	v_med3_f32 v249, v149, s77, v252
	v_med3_f32 v250, v150, s77, v252
	v_med3_f32 v251, v151, s77, v252
	v_mov_b32_e32 v246, v245
	v_cvt_pk_fp8_f32 v246, v248, v249
	v_cvt_pk_fp8_f32 v246, v250, v251 op_sel:[0,0,1]
	ds_write_b32 v38, v246 offset:64
	v_med3_f32 v248, v144, s77, v252
	v_med3_f32 v249, v145, s77, v252
	v_med3_f32 v250, v146, s77, v252
	v_med3_f32 v251, v147, s77, v252
	v_mov_b32_e32 v246, v245
	v_cvt_pk_fp8_f32 v246, v248, v249
	v_cvt_pk_fp8_f32 v246, v250, v251 op_sel:[0,0,1]
	ds_write_b32 v38, v246 offset:80
	v_med3_f32 v248, v140, s77, v252
	v_med3_f32 v249, v141, s77, v252
	v_med3_f32 v250, v142, s77, v252
	v_med3_f32 v251, v143, s77, v252
	v_mov_b32_e32 v246, v245
	v_cvt_pk_fp8_f32 v246, v248, v249
	v_cvt_pk_fp8_f32 v246, v250, v251 op_sel:[0,0,1]
	ds_write_b32 v38, v246 offset:96
	v_med3_f32 v248, v136, s77, v252
	v_med3_f32 v249, v137, s77, v252
	v_med3_f32 v250, v138, s77, v252
	v_med3_f32 v251, v139, s77, v252
	v_mov_b32_e32 v246, v245
	v_cvt_pk_fp8_f32 v246, v248, v249
	v_cvt_pk_fp8_f32 v246, v250, v251 op_sel:[0,0,1]
	ds_write_b32 v38, v246 offset:112

.Lt8zs_0:
	s_waitcnt vmcnt(4)
	ds_write_b128 v242, v[204:207]
	ds_write_b128 v242, v[208:211] offset:128
	ds_write_b128 v242, v[212:215] offset:2176
	ds_write_b128 v242, v[216:219] offset:2304
	ds_write_b128 v242, v[220:223] offset:4352
	ds_write_b128 v242, v[224:227] offset:4480
	ds_write_b128 v242, v[228:231] offset:6528
	ds_write_b128 v242, v[232:235] offset:6656
	global_load_dwordx4 v[204:207], v201, s[22:23] offset:512
	global_load_dwordx4 v[208:211], v201, s[22:23] offset:640
	global_load_dwordx4 v[212:215], v202, s[22:23] offset:512
	global_load_dwordx4 v[216:219], v202, s[22:23] offset:640
	global_load_dwordx4 v[220:223], v201, s[24:25] offset:512
	global_load_dwordx4 v[224:227], v201, s[24:25] offset:640
	global_load_dwordx4 v[228:231], v202, s[24:25] offset:512
	global_load_dwordx4 v[232:235], v202, s[24:25] offset:640
	s_waitcnt lgkmcnt(0)
	ds_read_b64 v[10:11], v243
	ds_read_b64 v[12:13], v243 offset:4352
	ds_read_b64 v[14:15], v243 offset:32
	ds_read_b64 v[16:17], v243 offset:4384
	ds_read_b64 v[18:19], v243 offset:64
	ds_read_b64 v[20:21], v243 offset:4416
	ds_read_b64 v[22:23], v243 offset:96
	ds_read_b64 v[24:25], v243 offset:4448
	ds_read_b64 v[26:27], v243 offset:128
	ds_read_b64 v[28:29], v243 offset:4480
	ds_read_b64 v[30:31], v243 offset:160
	ds_read_b64 v[32:33], v243 offset:4512
	ds_read_b64 v[34:35], v243 offset:192
	ds_read_b64 v[36:37], v243 offset:4544
	ds_read_b64 v[236:237], v243 offset:224
	ds_read_b64 v[238:239], v243 offset:4576
	s_waitcnt lgkmcnt(0)
	v_lshlrev_b32_e32 v168, 16, v10
	v_and_b32_e32 v169, 0xffff0000, v10
	v_lshlrev_b32_e32 v170, 16, v11
	v_and_b32_e32 v171, 0xffff0000, v11
	v_lshlrev_b32_e32 v172, 16, v12
	v_and_b32_e32 v173, 0xffff0000, v12
	v_lshlrev_b32_e32 v174, 16, v13
	v_and_b32_e32 v175, 0xffff0000, v13
	v_pk_mul_f32 v[168:169], v[4:5], v[168:169] op_sel_hi:[0,1]
	v_pk_mul_f32 v[170:171], v[4:5], v[170:171] op_sel_hi:[0,1]
	v_pk_fma_f32 v[132:133], v[184:185], v[132:133], v[168:169] op_sel_hi:[0,1,1]
	v_pk_fma_f32 v[134:135], v[184:185], v[134:135], v[170:171] op_sel_hi:[0,1,1]
	v_pk_mul_f32 v[132:133], v[132:133], v[172:173]
	v_pk_mul_f32 v[134:135], v[134:135], v[174:175]
	v_cvt_pk_bf16_f32 v240, v132, v133
	v_cvt_pk_bf16_f32 v241, v134, v135
	ds_write_b64 v0, v[240:241]
	v_lshlrev_b32_e32 v168, 16, v14
	v_and_b32_e32 v169, 0xffff0000, v14
	v_lshlrev_b32_e32 v170, 16, v15
	v_and_b32_e32 v171, 0xffff0000, v15
	v_lshlrev_b32_e32 v172, 16, v16
	v_and_b32_e32 v173, 0xffff0000, v16
	v_lshlrev_b32_e32 v174, 16, v17
	v_and_b32_e32 v175, 0xffff0000, v17
	v_pk_mul_f32 v[168:169], v[4:5], v[168:169] op_sel_hi:[0,1]
	v_pk_mul_f32 v[170:171], v[4:5], v[170:171] op_sel_hi:[0,1]
	v_pk_fma_f32 v[128:129], v[184:185], v[128:129], v[168:169] op_sel_hi:[0,1,1]
	v_pk_fma_f32 v[130:131], v[184:185], v[130:131], v[170:171] op_sel_hi:[0,1,1]
	v_pk_mul_f32 v[128:129], v[128:129], v[172:173]
	v_pk_mul_f32 v[130:131], v[130:131], v[174:175]
	v_cvt_pk_bf16_f32 v240, v128, v129
	v_cvt_pk_bf16_f32 v241, v130, v131
	ds_write_b64 v0, v[240:241] offset:32
	v_lshlrev_b32_e32 v168, 16, v18
	v_and_b32_e32 v169, 0xffff0000, v18
	v_lshlrev_b32_e32 v170, 16, v19
	v_and_b32_e32 v171, 0xffff0000, v19
	v_lshlrev_b32_e32 v172, 16, v20
	v_and_b32_e32 v173, 0xffff0000, v20
	v_lshlrev_b32_e32 v174, 16, v21
	v_and_b32_e32 v175, 0xffff0000, v21
	v_pk_mul_f32 v[168:169], v[4:5], v[168:169] op_sel_hi:[0,1]
	v_pk_mul_f32 v[170:171], v[4:5], v[170:171] op_sel_hi:[0,1]
	v_pk_fma_f32 v[124:125], v[184:185], v[124:125], v[168:169] op_sel_hi:[0,1,1]
	v_pk_fma_f32 v[126:127], v[184:185], v[126:127], v[170:171] op_sel_hi:[0,1,1]
	v_pk_mul_f32 v[124:125], v[124:125], v[172:173]
	v_pk_mul_f32 v[126:127], v[126:127], v[174:175]
	v_cvt_pk_bf16_f32 v240, v124, v125
	v_cvt_pk_bf16_f32 v241, v126, v127
	ds_write_b64 v0, v[240:241] offset:64
	v_lshlrev_b32_e32 v168, 16, v22
	v_and_b32_e32 v169, 0xffff0000, v22
	v_lshlrev_b32_e32 v170, 16, v23
	v_and_b32_e32 v171, 0xffff0000, v23
	v_lshlrev_b32_e32 v172, 16, v24
	v_and_b32_e32 v173, 0xffff0000, v24
	v_lshlrev_b32_e32 v174, 16, v25
	v_and_b32_e32 v175, 0xffff0000, v25
	v_pk_mul_f32 v[168:169], v[4:5], v[168:169] op_sel_hi:[0,1]
	v_pk_mul_f32 v[170:171], v[4:5], v[170:171] op_sel_hi:[0,1]
	v_pk_fma_f32 v[120:121], v[184:185], v[120:121], v[168:169] op_sel_hi:[0,1,1]
	v_pk_fma_f32 v[122:123], v[184:185], v[122:123], v[170:171] op_sel_hi:[0,1,1]
	v_pk_mul_f32 v[120:121], v[120:121], v[172:173]
	v_pk_mul_f32 v[122:123], v[122:123], v[174:175]
	v_cvt_pk_bf16_f32 v240, v120, v121
	v_cvt_pk_bf16_f32 v241, v122, v123
	ds_write_b64 v0, v[240:241] offset:96
	ds_read_b128 v[168:171], v1
	ds_read_b128 v[172:175], v1 offset:1152
	s_cbranch_vccz .Lt8z_1_0
	v_med3_f32 v248, v132, s77, v252
	v_med3_f32 v249, v133, s77, v252
	v_med3_f32 v250, v134, s77, v252
	v_med3_f32 v251, v135, s77, v252
	v_mov_b32_e32 v246, v245
	v_cvt_pk_fp8_f32 v246, v248, v249
	v_cvt_pk_fp8_f32 v246, v250, v251 op_sel:[0,0,1]
	ds_write_b32 v38, v246
	v_med3_f32 v248, v128, s77, v252
	v_med3_f32 v249, v129, s77, v252
	v_med3_f32 v250, v130, s77, v252
	v_med3_f32 v251, v131, s77, v252
	v_mov_b32_e32 v246, v245
	v_cvt_pk_fp8_f32 v246, v248, v249
	v_cvt_pk_fp8_f32 v246, v250, v251 op_sel:[0,0,1]
	ds_write_b32 v38, v246 offset:16
	v_med3_f32 v248, v124, s77, v252
	v_med3_f32 v249, v125, s77, v252
	v_med3_f32 v250, v126, s77, v252
	v_med3_f32 v251, v127, s77, v252
	v_mov_b32_e32 v246, v245
	v_cvt_pk_fp8_f32 v246, v248, v249
	v_cvt_pk_fp8_f32 v246, v250, v251 op_sel:[0,0,1]
	ds_write_b32 v38, v246 offset:32
	v_med3_f32 v248, v120, s77, v252
	v_med3_f32 v249, v121, s77, v252
	v_med3_f32 v250, v122, s77, v252
	v_med3_f32 v251, v123, s77, v252
	v_mov_b32_e32 v246, v245
	v_cvt_pk_fp8_f32 v246, v248, v249
	v_cvt_pk_fp8_f32 v246, v250, v251 op_sel:[0,0,1]
	ds_write_b32 v38, v246 offset:48

.Lt8zs_1:
	s_waitcnt vmcnt(4)
	ds_write_b128 v242, v[204:207]
	ds_write_b128 v242, v[208:211] offset:128
	ds_write_b128 v242, v[212:215] offset:2176
	ds_write_b128 v242, v[216:219] offset:2304
	ds_write_b128 v242, v[220:223] offset:4352
	ds_write_b128 v242, v[224:227] offset:4480
	ds_write_b128 v242, v[228:231] offset:6528
	ds_write_b128 v242, v[232:235] offset:6656
	global_load_dwordx4 v[204:207], v201, s[22:23] offset:768
	global_load_dwordx4 v[208:211], v201, s[22:23] offset:896
	global_load_dwordx4 v[212:215], v202, s[22:23] offset:768
	global_load_dwordx4 v[216:219], v202, s[22:23] offset:896
	global_load_dwordx4 v[220:223], v201, s[24:25] offset:768
	global_load_dwordx4 v[224:227], v201, s[24:25] offset:896
	global_load_dwordx4 v[228:231], v202, s[24:25] offset:768
	global_load_dwordx4 v[232:235], v202, s[24:25] offset:896
	s_waitcnt lgkmcnt(0)
	ds_read_b64 v[10:11], v243
	ds_read_b64 v[12:13], v243 offset:4352
	ds_read_b64 v[14:15], v243 offset:32
	ds_read_b64 v[16:17], v243 offset:4384
	ds_read_b64 v[18:19], v243 offset:64
	ds_read_b64 v[20:21], v243 offset:4416
	ds_read_b64 v[22:23], v243 offset:96
	ds_read_b64 v[24:25], v243 offset:4448
	ds_read_b64 v[26:27], v243 offset:128
	ds_read_b64 v[28:29], v243 offset:4480
	ds_read_b64 v[30:31], v243 offset:160
	ds_read_b64 v[32:33], v243 offset:4512
	ds_read_b64 v[34:35], v243 offset:192
	ds_read_b64 v[36:37], v243 offset:4544
	ds_read_b64 v[236:237], v243 offset:224
	ds_read_b64 v[238:239], v243 offset:4576
	s_waitcnt lgkmcnt(0)
	v_lshlrev_b32_e32 v168, 16, v10
	v_and_b32_e32 v169, 0xffff0000, v10
	v_lshlrev_b32_e32 v170, 16, v11
	v_and_b32_e32 v171, 0xffff0000, v11
	v_lshlrev_b32_e32 v172, 16, v12
	v_and_b32_e32 v173, 0xffff0000, v12
	v_lshlrev_b32_e32 v174, 16, v13
	v_and_b32_e32 v175, 0xffff0000, v13
	v_pk_mul_f32 v[168:169], v[4:5], v[168:169] op_sel_hi:[0,1]
	v_pk_mul_f32 v[170:171], v[4:5], v[170:171] op_sel_hi:[0,1]
	v_pk_fma_f32 v[100:101], v[184:185], v[100:101], v[168:169] op_sel_hi:[0,1,1]
	v_pk_fma_f32 v[102:103], v[184:185], v[102:103], v[170:171] op_sel_hi:[0,1,1]
	v_pk_mul_f32 v[100:101], v[100:101], v[172:173]
	v_pk_mul_f32 v[102:103], v[102:103], v[174:175]
	v_cvt_pk_bf16_f32 v240, v100, v101
	v_cvt_pk_bf16_f32 v241, v102, v103
	ds_write_b64 v0, v[240:241]
	v_lshlrev_b32_e32 v168, 16, v14
	v_and_b32_e32 v169, 0xffff0000, v14
	v_lshlrev_b32_e32 v170, 16, v15
	v_and_b32_e32 v171, 0xffff0000, v15
	v_lshlrev_b32_e32 v172, 16, v16
	v_and_b32_e32 v173, 0xffff0000, v16
	v_lshlrev_b32_e32 v174, 16, v17
	v_and_b32_e32 v175, 0xffff0000, v17
	v_pk_mul_f32 v[168:169], v[4:5], v[168:169] op_sel_hi:[0,1]
	v_pk_mul_f32 v[170:171], v[4:5], v[170:171] op_sel_hi:[0,1]
	v_pk_fma_f32 v[96:97], v[184:185], v[96:97], v[168:169] op_sel_hi:[0,1,1]
	v_pk_fma_f32 v[98:99], v[184:185], v[98:99], v[170:171] op_sel_hi:[0,1,1]
	v_pk_mul_f32 v[96:97], v[96:97], v[172:173]
	v_pk_mul_f32 v[98:99], v[98:99], v[174:175]
	v_cvt_pk_bf16_f32 v240, v96, v97
	v_cvt_pk_bf16_f32 v241, v98, v99
	ds_write_b64 v0, v[240:241] offset:32
	v_lshlrev_b32_e32 v168, 16, v18
	v_and_b32_e32 v169, 0xffff0000, v18
	v_lshlrev_b32_e32 v170, 16, v19
	v_and_b32_e32 v171, 0xffff0000, v19
	v_lshlrev_b32_e32 v172, 16, v20
	v_and_b32_e32 v173, 0xffff0000, v20
	v_lshlrev_b32_e32 v174, 16, v21
	v_and_b32_e32 v175, 0xffff0000, v21
	v_pk_mul_f32 v[168:169], v[4:5], v[168:169] op_sel_hi:[0,1]
	v_pk_mul_f32 v[170:171], v[4:5], v[170:171] op_sel_hi:[0,1]
	v_pk_fma_f32 v[92:93], v[184:185], v[92:93], v[168:169] op_sel_hi:[0,1,1]
	v_pk_fma_f32 v[94:95], v[184:185], v[94:95], v[170:171] op_sel_hi:[0,1,1]
	v_pk_mul_f32 v[92:93], v[92:93], v[172:173]
	v_pk_mul_f32 v[94:95], v[94:95], v[174:175]
	v_cvt_pk_bf16_f32 v240, v92, v93
	v_cvt_pk_bf16_f32 v241, v94, v95
	ds_write_b64 v0, v[240:241] offset:64
	v_lshlrev_b32_e32 v168, 16, v22
	v_and_b32_e32 v169, 0xffff0000, v22
	v_lshlrev_b32_e32 v170, 16, v23
	v_and_b32_e32 v171, 0xffff0000, v23
	v_lshlrev_b32_e32 v172, 16, v24
	v_and_b32_e32 v173, 0xffff0000, v24
	v_lshlrev_b32_e32 v174, 16, v25
	v_and_b32_e32 v175, 0xffff0000, v25
	v_pk_mul_f32 v[168:169], v[4:5], v[168:169] op_sel_hi:[0,1]
	v_pk_mul_f32 v[170:171], v[4:5], v[170:171] op_sel_hi:[0,1]
	v_pk_fma_f32 v[88:89], v[184:185], v[88:89], v[168:169] op_sel_hi:[0,1,1]
	v_pk_fma_f32 v[90:91], v[184:185], v[90:91], v[170:171] op_sel_hi:[0,1,1]
	v_pk_mul_f32 v[88:89], v[88:89], v[172:173]
	v_pk_mul_f32 v[90:91], v[90:91], v[174:175]
	v_cvt_pk_bf16_f32 v240, v88, v89
	v_cvt_pk_bf16_f32 v241, v90, v91
	ds_write_b64 v0, v[240:241] offset:96
	ds_read_b128 v[168:171], v1
	ds_read_b128 v[172:175], v1 offset:1152
	s_cbranch_vccz .Lt8z_2_0
	v_med3_f32 v248, v100, s77, v252
	v_med3_f32 v249, v101, s77, v252
	v_med3_f32 v250, v102, s77, v252
	v_med3_f32 v251, v103, s77, v252
	v_mov_b32_e32 v246, v245
	v_cvt_pk_fp8_f32 v246, v248, v249
	v_cvt_pk_fp8_f32 v246, v250, v251 op_sel:[0,0,1]
	ds_write_b32 v38, v246
	v_med3_f32 v248, v96, s77, v252
	v_med3_f32 v249, v97, s77, v252
	v_med3_f32 v250, v98, s77, v252
	v_med3_f32 v251, v99, s77, v252
	v_mov_b32_e32 v246, v245
	v_cvt_pk_fp8_f32 v246, v248, v249
	v_cvt_pk_fp8_f32 v246, v250, v251 op_sel:[0,0,1]
	ds_write_b32 v38, v246 offset:16
	v_med3_f32 v248, v92, s77, v252
	v_med3_f32 v249, v93, s77, v252
	v_med3_f32 v250, v94, s77, v252
	v_med3_f32 v251, v95, s77, v252
	v_mov_b32_e32 v246, v245
	v_cvt_pk_fp8_f32 v246, v248, v249
	v_cvt_pk_fp8_f32 v246, v250, v251 op_sel:[0,0,1]
	ds_write_b32 v38, v246 offset:32
	v_med3_f32 v248, v88, s77, v252
	v_med3_f32 v249, v89, s77, v252
	v_med3_f32 v250, v90, s77, v252
	v_med3_f32 v251, v91, s77, v252
	v_mov_b32_e32 v246, v245
	v_cvt_pk_fp8_f32 v246, v248, v249
	v_cvt_pk_fp8_f32 v246, v250, v251 op_sel:[0,0,1]
	ds_write_b32 v38, v246 offset:48
.Lt8z_2_0:
	s_waitcnt lgkmcnt(0)
	global_store_dwordx4 v[194:195], v[168:171], off offset:512
	global_store_dwordx4 v[196:197], v[172:175], off offset:512
	s_nop 1
	v_lshlrev_b32_e32 v168, 16, v26
	v_and_b32_e32 v169, 0xffff0000, v26
	v_lshlrev_b32_e32 v170, 16, v27
	v_and_b32_e32 v171, 0xffff0000, v27
	v_lshlrev_b32_e32 v172, 16, v28
	v_and_b32_e32 v173, 0xffff0000, v28
	v_lshlrev_b32_e32 v174, 16, v29
	v_and_b32_e32 v175, 0xffff0000, v29
	v_pk_mul_f32 v[168:169], v[4:5], v[168:169] op_sel_hi:[0,1]
	v_pk_mul_f32 v[170:171], v[4:5], v[170:171] op_sel_hi:[0,1]
	v_pk_fma_f32 v[84:85], v[184:185], v[84:85], v[168:169] op_sel_hi:[0,1,1]
	v_pk_fma_f32 v[86:87], v[184:185], v[86:87], v[170:171] op_sel_hi:[0,1,1]
	v_pk_mul_f32 v[84:85], v[84:85], v[172:173]
	v_pk_mul_f32 v[86:87], v[86:87], v[174:175]
	v_cvt_pk_bf16_f32 v240, v84, v85
	v_cvt_pk_bf16_f32 v241, v86, v87
	ds_write_b64 v0, v[240:241]
	v_lshlrev_b32_e32 v168, 16, v30
	v_and_b32_e32 v169, 0xffff0000, v30
	v_lshlrev_b32_e32 v170, 16, v31
	v_and_b32_e32 v171, 0xffff0000, v31
	v_lshlrev_b32_e32 v172, 16, v32
	v_and_b32_e32 v173, 0xffff0000, v32
	v_lshlrev_b32_e32 v174, 16, v33
	v_and_b32_e32 v175, 0xffff0000, v33
	v_pk_mul_f32 v[168:169], v[4:5], v[168:169] op_sel_hi:[0,1]
	v_pk_mul_f32 v[170:171], v[4:5], v[170:171] op_sel_hi:[0,1]
	v_pk_fma_f32 v[80:81], v[184:185], v[80:81], v[168:169] op_sel_hi:[0,1,1]
	v_pk_fma_f32 v[82:83], v[184:185], v[82:83], v[170:171] op_sel_hi:[0,1,1]
	v_pk_mul_f32 v[80:81], v[80:81], v[172:173]
	v_pk_mul_f32 v[82:83], v[82:83], v[174:175]
	v_cvt_pk_bf16_f32 v240, v80, v81
	v_cvt_pk_bf16_f32 v241, v82, v83
	ds_write_b64 v0, v[240:241] offset:32
	v_lshlrev_b32_e32 v168, 16, v34
	v_and_b32_e32 v169, 0xffff0000, v34
	v_lshlrev_b32_e32 v170, 16, v35
	v_and_b32_e32 v171, 0xffff0000, v35
	v_lshlrev_b32_e32 v172, 16, v36
	v_and_b32_e32 v173, 0xffff0000, v36
	v_lshlrev_b32_e32 v174, 16, v37
	v_and_b32_e32 v175, 0xffff0000, v37
	v_pk_mul_f32 v[168:169], v[4:5], v[168:169] op_sel_hi:[0,1]
	v_pk_mul_f32 v[170:171], v[4:5], v[170:171] op_sel_hi:[0,1]
	v_pk_fma_f32 v[76:77], v[184:185], v[76:77], v[168:169] op_sel_hi:[0,1,1]
	v_pk_fma_f32 v[78:79], v[184:185], v[78:79], v[170:171] op_sel_hi:[0,1,1]
	v_pk_mul_f32 v[76:77], v[76:77], v[172:173]
	v_pk_mul_f32 v[78:79], v[78:79], v[174:175]
	v_cvt_pk_bf16_f32 v240, v76, v77
	v_cvt_pk_bf16_f32 v241, v78, v79
	ds_write_b64 v0, v[240:241] offset:64
	v_lshlrev_b32_e32 v168, 16, v236
	v_and_b32_e32 v169, 0xffff0000, v236
	v_lshlrev_b32_e32 v170, 16, v237
	v_and_b32_e32 v171, 0xffff0000, v237
	v_lshlrev_b32_e32 v172, 16, v238
	v_and_b32_e32 v173, 0xffff0000, v238
	v_lshlrev_b32_e32 v174, 16, v239
	v_and_b32_e32 v175, 0xffff0000, v239
	v_pk_mul_f32 v[168:169], v[4:5], v[168:169] op_sel_hi:[0,1]
	v_pk_mul_f32 v[170:171], v[4:5], v[170:171] op_sel_hi:[0,1]
	v_pk_fma_f32 v[72:73], v[184:185], v[72:73], v[168:169] op_sel_hi:[0,1,1]
	v_pk_fma_f32 v[74:75], v[184:185], v[74:75], v[170:171] op_sel_hi:[0,1,1]
	v_pk_mul_f32 v[72:73], v[72:73], v[172:173]
	v_pk_mul_f32 v[74:75], v[74:75], v[174:175]
	v_cvt_pk_bf16_f32 v240, v72, v73
	v_cvt_pk_bf16_f32 v241, v74, v75
	ds_write_b64 v0, v[240:241] offset:96
	ds_read_b128 v[168:171], v1
	ds_read_b128 v[172:175], v1 offset:1152
	s_cbranch_vccz .Lt8z_2_1
	v_med3_f32 v248, v84, s77, v252
	v_med3_f32 v249, v85, s77, v252
	v_med3_f32 v250, v86, s77, v252
	v_med3_f32 v251, v87, s77, v252
	v_mov_b32_e32 v246, v245
	v_cvt_pk_fp8_f32 v246, v248, v249
	v_cvt_pk_fp8_f32 v246, v250, v251 op_sel:[0,0,1]
	ds_write_b32 v38, v246 offset:64
	v_med3_f32 v248, v80, s77, v252
	v_med3_f32 v249, v81, s77, v252
	v_med3_f32 v250, v82, s77, v252
	v_med3_f32 v251, v83, s77, v252
	v_mov_b32_e32 v246, v245
	v_cvt_pk_fp8_f32 v246, v248, v249
	v_cvt_pk_fp8_f32 v246, v250, v251 op_sel:[0,0,1]
	ds_write_b32 v38, v246 offset:80
	v_med3_f32 v248, v76, s77, v252
	v_med3_f32 v249, v77, s77, v252
	v_med3_f32 v250, v78, s77, v252
	v_med3_f32 v251, v79, s77, v252
	v_mov_b32_e32 v246, v245
	v_cvt_pk_fp8_f32 v246, v248, v249
	v_cvt_pk_fp8_f32 v246, v250, v251 op_sel:[0,0,1]
	ds_write_b32 v38, v246 offset:96
	v_med3_f32 v248, v72, s77, v252
	v_med3_f32 v249, v73, s77, v252
	v_med3_f32 v250, v74, s77, v252
	v_med3_f32 v251, v75, s77, v252
	v_mov_b32_e32 v246, v245
	v_cvt_pk_fp8_f32 v246, v248, v249
	v_cvt_pk_fp8_f32 v246, v250, v251 op_sel:[0,0,1]
	ds_write_b32 v38, v246 offset:112

.Lt8zs_2:
	s_waitcnt vmcnt(4)
	ds_write_b128 v242, v[204:207]
	ds_write_b128 v242, v[208:211] offset:128
	ds_write_b128 v242, v[212:215] offset:2176
	ds_write_b128 v242, v[216:219] offset:2304
	ds_write_b128 v242, v[220:223] offset:4352
	ds_write_b128 v242, v[224:227] offset:4480
	ds_write_b128 v242, v[228:231] offset:6528
	ds_write_b128 v242, v[232:235] offset:6656
	s_waitcnt lgkmcnt(0)
	ds_read_b64 v[10:11], v243
	ds_read_b64 v[12:13], v243 offset:4352
	ds_read_b64 v[14:15], v243 offset:32
	ds_read_b64 v[16:17], v243 offset:4384
	ds_read_b64 v[18:19], v243 offset:64
	ds_read_b64 v[20:21], v243 offset:4416
	ds_read_b64 v[22:23], v243 offset:96
	ds_read_b64 v[24:25], v243 offset:4448
	ds_read_b64 v[26:27], v243 offset:128
	ds_read_b64 v[28:29], v243 offset:4480
	ds_read_b64 v[30:31], v243 offset:160
	ds_read_b64 v[32:33], v243 offset:4512
	ds_read_b64 v[34:35], v243 offset:192
	ds_read_b64 v[36:37], v243 offset:4544
	ds_read_b64 v[236:237], v243 offset:224
	ds_read_b64 v[238:239], v243 offset:4576
	s_waitcnt lgkmcnt(0)
	v_lshlrev_b32_e32 v168, 16, v10
	v_and_b32_e32 v169, 0xffff0000, v10
	v_lshlrev_b32_e32 v170, 16, v11
	v_and_b32_e32 v171, 0xffff0000, v11
	v_lshlrev_b32_e32 v172, 16, v12
	v_and_b32_e32 v173, 0xffff0000, v12
	v_lshlrev_b32_e32 v174, 16, v13
	v_and_b32_e32 v175, 0xffff0000, v13
	v_pk_mul_f32 v[168:169], v[4:5], v[168:169] op_sel_hi:[0,1]
	v_pk_mul_f32 v[170:171], v[4:5], v[170:171] op_sel_hi:[0,1]
	v_pk_fma_f32 v[68:69], v[184:185], v[68:69], v[168:169] op_sel_hi:[0,1,1]
	v_pk_fma_f32 v[70:71], v[184:185], v[70:71], v[170:171] op_sel_hi:[0,1,1]
	v_pk_mul_f32 v[68:69], v[68:69], v[172:173]
	v_pk_mul_f32 v[70:71], v[70:71], v[174:175]
	v_cvt_pk_bf16_f32 v240, v68, v69
	v_cvt_pk_bf16_f32 v241, v70, v71
	ds_write_b64 v0, v[240:241]
	v_lshlrev_b32_e32 v168, 16, v14
	v_and_b32_e32 v169, 0xffff0000, v14
	v_lshlrev_b32_e32 v170, 16, v15
	v_and_b32_e32 v171, 0xffff0000, v15
	v_lshlrev_b32_e32 v172, 16, v16
	v_and_b32_e32 v173, 0xffff0000, v16
	v_lshlrev_b32_e32 v174, 16, v17
	v_and_b32_e32 v175, 0xffff0000, v17
	v_pk_mul_f32 v[168:169], v[4:5], v[168:169] op_sel_hi:[0,1]
	v_pk_mul_f32 v[170:171], v[4:5], v[170:171] op_sel_hi:[0,1]
	v_pk_fma_f32 v[64:65], v[184:185], v[64:65], v[168:169] op_sel_hi:[0,1,1]
	v_pk_fma_f32 v[66:67], v[184:185], v[66:67], v[170:171] op_sel_hi:[0,1,1]
	v_pk_mul_f32 v[64:65], v[64:65], v[172:173]
	v_pk_mul_f32 v[66:67], v[66:67], v[174:175]
	v_cvt_pk_bf16_f32 v240, v64, v65
	v_cvt_pk_bf16_f32 v241, v66, v67
	ds_write_b64 v0, v[240:241] offset:32
	v_lshlrev_b32_e32 v168, 16, v18
	v_and_b32_e32 v169, 0xffff0000, v18
	v_lshlrev_b32_e32 v170, 16, v19
	v_and_b32_e32 v171, 0xffff0000, v19
	v_lshlrev_b32_e32 v172, 16, v20
	v_and_b32_e32 v173, 0xffff0000, v20
	v_lshlrev_b32_e32 v174, 16, v21
	v_and_b32_e32 v175, 0xffff0000, v21
	v_pk_mul_f32 v[168:169], v[4:5], v[168:169] op_sel_hi:[0,1]
	v_pk_mul_f32 v[170:171], v[4:5], v[170:171] op_sel_hi:[0,1]
	v_pk_fma_f32 v[60:61], v[184:185], v[60:61], v[168:169] op_sel_hi:[0,1,1]
	v_pk_fma_f32 v[62:63], v[184:185], v[62:63], v[170:171] op_sel_hi:[0,1,1]
	v_pk_mul_f32 v[60:61], v[60:61], v[172:173]
	v_pk_mul_f32 v[62:63], v[62:63], v[174:175]
	v_cvt_pk_bf16_f32 v240, v60, v61
	v_cvt_pk_bf16_f32 v241, v62, v63
	ds_write_b64 v0, v[240:241] offset:64
	v_lshlrev_b32_e32 v168, 16, v22
	v_and_b32_e32 v169, 0xffff0000, v22
	v_lshlrev_b32_e32 v170, 16, v23
	v_and_b32_e32 v171, 0xffff0000, v23
	v_lshlrev_b32_e32 v172, 16, v24
	v_and_b32_e32 v173, 0xffff0000, v24
	v_lshlrev_b32_e32 v174, 16, v25
	v_and_b32_e32 v175, 0xffff0000, v25
	v_pk_mul_f32 v[168:169], v[4:5], v[168:169] op_sel_hi:[0,1]
	v_pk_mul_f32 v[170:171], v[4:5], v[170:171] op_sel_hi:[0,1]
	v_pk_fma_f32 v[56:57], v[184:185], v[56:57], v[168:169] op_sel_hi:[0,1,1]
	v_pk_fma_f32 v[58:59], v[184:185], v[58:59], v[170:171] op_sel_hi:[0,1,1]
	v_pk_mul_f32 v[56:57], v[56:57], v[172:173]
	v_pk_mul_f32 v[58:59], v[58:59], v[174:175]
	v_cvt_pk_bf16_f32 v240, v56, v57
	v_cvt_pk_bf16_f32 v241, v58, v59
	ds_write_b64 v0, v[240:241] offset:96
	ds_read_b128 v[168:171], v1
	ds_read_b128 v[172:175], v1 offset:1152
	s_cbranch_vccz .Lt8z_3_0
	v_med3_f32 v248, v68, s77, v252
	v_med3_f32 v249, v69, s77, v252
	v_med3_f32 v250, v70, s77, v252
	v_med3_f32 v251, v71, s77, v252
	v_mov_b32_e32 v246, v245
	v_cvt_pk_fp8_f32 v246, v248, v249
	v_cvt_pk_fp8_f32 v246, v250, v251 op_sel:[0,0,1]
	ds_write_b32 v38, v246
	v_med3_f32 v248, v64, s77, v252
	v_med3_f32 v249, v65, s77, v252
	v_med3_f32 v250, v66, s77, v252
	v_med3_f32 v251, v67, s77, v252
	v_mov_b32_e32 v246, v245
	v_cvt_pk_fp8_f32 v246, v248, v249
	v_cvt_pk_fp8_f32 v246, v250, v251 op_sel:[0,0,1]
	ds_write_b32 v38, v246 offset:16
	v_med3_f32 v248, v60, s77, v252
	v_med3_f32 v249, v61, s77, v252
	v_med3_f32 v250, v62, s77, v252
	v_med3_f32 v251, v63, s77, v252
	v_mov_b32_e32 v246, v245
	v_cvt_pk_fp8_f32 v246, v248, v249
	v_cvt_pk_fp8_f32 v246, v250, v251 op_sel:[0,0,1]
	ds_write_b32 v38, v246 offset:32
	v_med3_f32 v248, v56, s77, v252
	v_med3_f32 v249, v57, s77, v252
	v_med3_f32 v250, v58, s77, v252
	v_med3_f32 v251, v59, s77, v252
	v_mov_b32_e32 v246, v245
	v_cvt_pk_fp8_f32 v246, v248, v249
	v_cvt_pk_fp8_f32 v246, v250, v251 op_sel:[0,0,1]
	ds_write_b32 v38, v246 offset:48
